# layer-1 down-projection weight conversion moved out of layer 0's in-projection tail into the workgroups idle at the end of layer 0's down-projection phase (same conversion loop re-entered); in-project
# speedup vs baseline: 1.0095x; 1.0065x over previous
; #define LAS __attribute__((address_space(3)))
; __device__ __forceinline__ int opaque_tid() { int t = threadIdx.x; asm volatile("" : "+v"(t)); return t; }
;     __device__ __forceinline__ bool next(int i, Unit& u) const {
;         const long L = (long)i * G + c; if (L >= nwg) return false;
;         int wgid = (int)L; { const int q = nwg / NXCD, r = nwg % NXCD, xcd = wgid % NXCD, off = wgid / NXCD; wgid = (xcd < r ? xcd * (q + 1) : r * (q + 1) + (xcd - r) * q) + off; }
;         const int nig = WGM * nN, gid = wgid / nig, fm = gid * WGM, gsz = (nM - fm) < WGM ? (nM - fm) : WGM;
;         u.pm = fm + ((wgid % nig) % gsz); u.pn = (wgid % nig) / gsz; u.e = 0; u.rows = 256;
;         u.a = A + (size_t)u.pm * tstepA; u.b = Bt + (size_t)u.pn * tstep; return true;
; __device__ __forceinline__ void pj_mfma(const Args& a, LAS unsigned char* lds, int layer) {
;     pg8::DenseOrder So; So.init(a.ws + WS_ACT, a.ws + WS_WIN + (size_t)layer * 3328 * D * 2, NTOK, 3328, D, gridDim.x, blockIdx.x);
;     LAS float* gl = (LAS float*)(lds + SEG_OFF + 256);
;     { const int t_ = opaque_tid(); if (t_ < 256) { const int w = t_ >> 6, i = t_ & 63; const float* gp_ = w == 0 ? a.in[I_QGF] : w == 1 ? a.in[I_KGF] : w == 2 ? a.in[I_QGD] : a.in[I_KGD]; gl[t_] = gp_[layer * 64 + i]; } }
;     __syncthreads();
;     EpiProj E{(bf16_t*)(a.ws + WS_PROJ), gl};
;     pg8::gemm_phase<EpiProj, pg8::DenseOrder>(lds, D, So, E);
;     if ((int)blockIdx.x >= (int)gridDim.x - 32) cumsum_unit(a, lds, blockIdx.x - (gridDim.x - 32));
;     if (layer + 1 < NL) { __syncthreads(); constexpr int I_SPLIT = 10240;
;         const int half = gridDim.x / 2; const bool upper = (int)blockIdx.x >= half;
;         p0_prep(a, lds, layer + 1, upper ? half : 0, upper ? (int)gridDim.x - half : half, upper ? 0 : I_SPLIT, upper ? I_SPLIT : (1 << 30)); }
.LBB0_101:
	s_or_b64 exec, exec, s[0:1]
	s_mov_b32 vcc_lo, 0
	s_nop 1
	v_writelane_b32 v254, vcc_lo, 60
	s_nop 1
	s_mov_b32 vcc_lo, 0
	s_nop 1
	v_writelane_b32 v254, vcc_lo, 62
	s_nop 1
	s_waitcnt lgkmcnt(0)
	s_barrier
	s_load_dwordx2 s[92:93], s[54:55], 0xa0
	s_load_dwordx16 s[12:27], s[54:55], 0x20
	s_load_dwordx4 s[0:3], s[54:55], 0x90
	s_movk_i32 s5, 0xd1
	s_mov_b32 s67, 0
	s_waitcnt vmcnt(0)
	v_mbcnt_lo_u32_b32 v1, -1, 0
	v_mbcnt_hi_u32_b32 v199, -1, v1
	s_waitcnt lgkmcnt(0)
	v_writelane_b32 v252, s0, 8
	v_and_b32_e32 v240, 64, v199
	s_mul_hi_u32 s85, s77, 0x600
	v_writelane_b32 v252, s1, 9
	v_writelane_b32 v252, s2, 10
	v_writelane_b32 v252, s3, 11
	s_add_u32 s0, s92, 0x100000
	s_addc_u32 s1, s93, 0
	v_writelane_b32 v252, s0, 12
	s_add_u32 s96, s92, 0xbc00000
	s_addc_u32 s97, s93, 0
	v_writelane_b32 v252, s1, 13
	s_lshl_b32 s0, s61, 3
	s_add_u32 s10, s92, 0x180000
	s_addc_u32 s11, s93, 0
	s_add_u32 s80, s92, 0x7c00000
	s_addc_u32 s81, s93, 0
	v_writelane_b32 v252, s0, 14
	s_add_u32 s0, s92, 0xfc00000
	s_addc_u32 s1, s93, 0
	s_add_u32 s50, s92, 0x18c00000
	s_addc_u32 s51, s93, 0
	s_add_u32 s2, s92, 0xa00000
	s_addc_u32 s3, s93, 0
	v_writelane_b32 v252, s2, 15
	s_cmpk_lt_i32 s61, 0x680
	s_mul_i32 s84, s77, 0x600
	v_writelane_b32 v252, s3, 16
	s_cselect_b64 s[2:3], -1, 0
	v_writelane_b32 v252, s2, 17
	v_mov_b32_e32 v35, 0
	v_add_u32_e32 v241, 64, v240
	v_writelane_b32 v252, s3, 18
	s_ashr_i32 s2, s61, 31
	v_writelane_b32 v252, s2, 19
	s_lshr_b32 s2, s2, 29
	s_add_i32 s3, s61, s2
	s_ashr_i32 s2, s3, 3
	s_and_b32 s3, s3, -8
	s_sub_i32 s3, s61, s3
	s_lshl_b32 s4, s3, 6
	s_cmp_lt_i32 s3, 0
	s_cselect_b32 s5, s5, 0xd0
	s_mul_i32 s5, s5, s3
	s_mulk_i32 s3, 0x41
	s_cselect_b32 s3, s3, s4
	s_add_i32 s5, s5, s2
	s_mul_hi_i32 s4, s5, 0x4ec4ec4f
	s_lshr_b32 s6, s4, 31
	s_ashr_i32 s4, s4, 5
	s_add_i32 s4, s4, s6
	s_mul_i32 s6, s4, 0x68
	s_sub_i32 s5, s5, s6
	s_lshl_b32 s7, s4, 3
	s_bfe_i32 s4, s5, 0x80000
	s_bfe_u32 s4, s4, 0x3000c
	s_add_i32 s6, s5, s4
	s_bfe_i32 s4, s6, 0x80000
	s_and_b32 s6, s6, 0xf8
	s_sub_i32 s5, s5, s6
	s_sext_i32_i16 s8, s4
	s_sext_i32_i8 s5, s5
	s_add_i32 s28, s7, s5
	s_ashr_i32 s5, s8, 3
	v_writelane_b32 v252, s5, 20
	s_mov_b32 s6, s28
	s_ashr_i32 s29, s28, 31
	v_writelane_b32 v252, s6, 21
	s_lshr_b32 s4, s8, 3
	v_xor_b32_e32 v236, 16, v199
	v_writelane_b32 v252, s7, 22
	s_lshl_b64 s[6:7], s[28:29], 19
	s_add_u32 s6, s80, s6
	s_addc_u32 s7, s81, s7
	v_writelane_b32 v252, s6, 23
	s_bfe_i64 s[4:5], s[4:5], 0x100000
	s_lshl_b64 s[4:5], s[4:5], 19
	v_writelane_b32 v252, s7, 24
	v_writelane_b32 v252, s4, 25
	v_xor_b32_e32 v237, 32, v199
	v_mov_b32_e32 v238, 1
	v_writelane_b32 v252, s5, 26
	s_ashr_i32 s4, s77, 31
	v_writelane_b32 v252, s4, 27
	s_sub_i32 s4, s77, 32
	s_cmp_ge_i32 s61, s4
	s_cselect_b64 s[6:7], -1, 0
	v_writelane_b32 v252, s6, 28
	s_sub_i32 s4, s61, s4
	s_and_b32 s5, s4, 3
	v_writelane_b32 v252, s7, 29
	s_ashr_i32 s6, s4, 2
	s_ashr_i32 s7, s6, 31
	s_lshl_b32 s5, s5, 2
	s_add_u32 s5, s10, s5
	v_writelane_b32 v252, s10, 30
	s_addc_u32 s8, s11, 0
	s_lshl_b64 s[6:7], s[6:7], 16
	s_add_u32 s6, s5, s6
	s_addc_u32 s7, s8, s7
	s_add_u32 s28, s92, 0x200000
	s_addc_u32 s29, s93, 0
	s_ashr_i32 s5, s4, 31
	s_lshl_b64 s[4:5], s[4:5], 14
	v_writelane_b32 v252, s11, 31
	s_add_u32 s4, s28, s4
	v_writelane_b32 v252, s6, 32
	s_addc_u32 s5, s29, s5
	s_lshr_b32 s8, s77, 1
	v_writelane_b32 v252, s7, 33
	s_sub_i32 s9, s77, s8
	v_writelane_b32 v252, s4, 34
	s_cmp_lt_i32 s61, s8
	v_mov_b32_e32 v198, 0x358637bd
	v_writelane_b32 v252, s5, 35
	s_cselect_b64 s[4:5], -1, 0
	s_and_b64 s[6:7], s[4:5], exec
	s_cselect_b32 s6, s8, s9
	s_movk_i32 s7, 0x2880
	s_cselect_b32 s10, 0, s8
	s_cselect_b32 s8, 0x1dc0, 0
	s_cselect_b32 s7, s7, 0x1dc0
	s_lshl_b32 s6, s6, 3
	v_writelane_b32 v252, s7, 36
	s_cmp_ge_i32 s61, s10
	v_writelane_b32 v252, s6, 37
	s_cselect_b64 s[6:7], -1, 0
	s_or_b64 s[4:5], s[36:37], s[4:5]
	s_load_dwordx8 s[36:43], s[54:55], 0x60
	s_and_b64 s[4:5], s[6:7], s[4:5]
	v_writelane_b32 v252, s4, 38
	v_mov_b32_e32 v201, 1.0
	v_mov_b32_e32 v239, 0x7f800000
	v_writelane_b32 v252, s5, 39
	s_sub_i32 s4, s61, s10
	s_lshl_b32 s4, s4, 3
	s_add_i32 s4, s4, s8
	s_waitcnt lgkmcnt(0)
	s_mov_b64 s[8:9], s[40:41]
	v_writelane_b32 v252, s4, 40
	s_add_u32 s6, s38, 0x400000
	s_mov_b64 s[10:11], s[42:43]
	s_mov_b64 s[4:5], s[36:37]
	v_writelane_b32 v252, s4, 41
	v_mov_b32_e32 v202, 0x3f317218
	v_mov_b32_e32 v242, 0xff800000
	v_writelane_b32 v252, s5, 42
	v_writelane_b32 v252, s6, 43
	v_writelane_b32 v252, s7, 44
	v_writelane_b32 v252, s8, 45
	v_writelane_b32 v252, s9, 46
	v_writelane_b32 v252, s10, 47
	v_writelane_b32 v252, s11, 48
	s_addc_u32 s7, s39, 0
	v_writelane_b32 v252, s6, 49
	s_add_u32 s4, s16, 0xd04000
	s_movk_i32 s74, 0x1ff
	v_writelane_b32 v252, s7, 50
	v_writelane_b32 v252, s12, 51
	s_addc_u32 s5, s17, 0
	s_mov_b32 s76, 0x800000
	v_writelane_b32 v255, s25, 0
	v_writelane_b32 v255, s26, 1
	v_writelane_b32 v255, s27, 2
	v_writelane_b32 v255, s4, 3
	v_writelane_b32 v252, s13, 52
	v_writelane_b32 v252, s14, 53
	v_writelane_b32 v255, s5, 4
	s_add_u32 s4, s92, 0x5b00000
	s_addc_u32 s5, s93, 0
	v_writelane_b32 v255, s4, 5
	v_writelane_b32 v252, s15, 54
	v_writelane_b32 v252, s16, 55
	v_writelane_b32 v255, s5, 6
	s_add_u32 s4, s92, 0x1b00000
	s_addc_u32 s5, s93, 0
	s_add_u32 s82, s92, 0x700000
	v_writelane_b32 v255, s4, 7
	s_addc_u32 s83, s93, 0
	v_writelane_b32 v252, s17, 56
	v_writelane_b32 v255, s5, 8
	s_add_u32 s4, s92, 0x14000
	v_writelane_b32 v255, s4, 9
	s_addc_u32 s4, s93, 0
	s_add_i32 s6, s61, 0x900
	s_cmpk_lt_i32 s61, 0x200
	v_writelane_b32 v255, s4, 10
	s_cselect_b64 s[4:5], -1, 0
	v_writelane_b32 v255, s4, 11
	v_writelane_b32 v252, s18, 57
;     ...
;         if (u < AT_NFOX) {
;             const int qb = 15 - (u >> 5), bh = u & 31, b = bh >> 2, h = bh & 3, q0 = qb * 256;
;             const size_t rb = (size_t)b * S;
;             const bf16_t* Kb = proj + ((size_t)(4 + h) * NTOK + rb) * 64;
;             const bf16_t* Vb = proj + ((size_t)(8 + h) * NTOK + rb) * 64;
;             const float* cum = cumall + (size_t)bh * S;
;             const int jhi = 4 * qb + 3;
;             fox_cr = cum[q0]; fox_cv = cum[64 * (lane <= jhi ? lane : jhi) + 63]; fox_cq = cum[q0 + 32 * wid + r32];
;             if (!(dbg & 1)) { FOX_ISSUE(0); FOX_ISSUE(1); FOX_ISSUE(2); }
;             const bf16_t* Q = proj + ((size_t)(0 + h) * NTOK + rb + q0 + 32 * wid + r32) * 64;
; #pragma unroll
;             for (int d0 = 0; d0 < 4; ++d0) qr[d0] = *(const bf16x8*)(Q + d0 * 16 + hi * 8);
;         } else if (u < AT_NFOX + AT_NDIL) {
;             const int v2 = u - AT_NFOX, bh = v2 % 48, rest = v2 / 48, b = bh / 6, h = bh % 6, p = rest >> 4, x = rest & 15;
;             const int dil = p == 0 ? 1 : p == 1 ? 4 : 16, res = x % dil, nb2 = x / dil;
;             const size_t rb = (size_t)b * S;
;             const bf16_t* Kb = proj + ((size_t)(22 + h) * NTOK + rb) * 64;
;             const bf16_t* Vb = proj + ((size_t)(28 + h) * NTOK + rb) * 64;
;             const int mk_base = 256 * nb2 - 128, tt_lo = nb2 == 0 ? 2 : 0;
;             const size_t rs = (size_t)64 * dil;
; #pragma unroll
;     ...
;             if (tid < 256) { const int st = tid - 64; tab[tid] = (st >= 0 && st <= 128) ? relb[t5_bucket(st * dil) * 6 + h] : -INFINITY; }
;             const size_t trow = (size_t)(256 * nb2 + 32 * wid + r32) * dil + res;
;             const bf16_t* Q = proj + ((size_t)(16 + h) * NTOK + rb + trow) * 64;
; #pragma unroll
;             for (int d0 = 0; d0 < 4; ++d0) qr[d0] = *(const bf16x8*)(Q + d0 * 16 + hi * 8);
;         } else {
;             const int v2 = u - AT_NFOX - AT_NDIL, qb = 15 - v2 / 48, bh = v2 % 48, b = bh / 6, h = bh % 6, q0 = qb * 256;
;             const size_t rb = (size_t)b * S;
;             const bf16_t* Kb = proj + ((size_t)(40 + h) * NTOK + rb) * 64;
;             const bf16_t* Vb = proj + ((size_t)(46 + h) * NTOK + rb) * 64;
;             const int jhi = (q0 + 254) >> 6;
;             if (!(dbg & 1)) { SB_ISSUE(0); SB_ISSUE(1); SB_ISSUE(2); }
	v_writelane_b32 v252, s19, 58
	v_writelane_b32 v255, s5, 12
	s_and_b64 s[4:5], s[4:5], exec
	s_cselect_b32 s13, s61, s6
	s_cmpk_lt_i32 s13, 0xe00
	s_cselect_b64 s[4:5], -1, 0
	v_writelane_b32 v255, s4, 13
	s_cmpk_gt_i32 s13, 0x1ff
	s_mov_b32 s17, s67
	v_writelane_b32 v255, s5, 14
	s_cselect_b64 s[4:5], -1, 0
	v_writelane_b32 v255, s4, 15
	s_cmpk_gt_u32 s13, 0xaff
	v_writelane_b32 v252, s20, 59
	v_writelane_b32 v255, s5, 16
	s_cselect_b64 s[4:5], -1, 0
	v_writelane_b32 v255, s4, 17
	v_writelane_b32 v252, s21, 60
	s_mov_b32 s21, s67
	v_writelane_b32 v255, s5, 18
	s_add_i32 s4, s13, 0xf500
	s_and_b32 s5, s4, 0xffff
	s_mul_i32 s5, s5, 0xaaab
	s_lshr_b32 s5, s5, 21
	s_mul_i32 s6, s5, 48
	s_sub_i32 s4, s4, s6
	s_and_b32 s6, s4, 0xff
	s_mulk_i32 s6, 0xab
	s_bfe_u32 s6, s6, 0x6000a
	s_mul_i32 s7, s6, 6
	s_sub_i32 s4, s4, s7
	s_and_b32 s4, s4, 0xff
	s_lshl_b32 s6, s6, 12
	s_lshl_b32 s4, s4, 15
	s_add_i32 s7, s6, s4
	s_lshl_b32 s7, s7, 7
	s_add_i32 s8, s7, 0xb800000
	s_add_u32 s8, s96, s8
	s_addc_u32 s9, s97, 0
	s_add_i32 s7, s7, 0xa000000
	s_add_u32 s7, s96, s7
	s_addc_u32 s10, s97, 0
	s_lshl_b32 s11, s5, 14
	s_sub_i32 s12, 0x3f000, s11
	s_lshl_b32 s12, s12, 1
	s_add_u32 s14, s7, s12
	s_addc_u32 s15, s10, 0
	v_writelane_b32 v255, s14, 19
	v_writelane_b32 v252, s22, 61
	v_writelane_b32 v252, s23, 62
	v_writelane_b32 v255, s15, 20
	s_add_u32 s14, s8, s12
	s_addc_u32 s15, s9, 0
	s_sub_i32 s12, 0x3e000, s11
	v_writelane_b32 v255, s14, 21
	s_lshl_b32 s12, s12, 1
	v_writelane_b32 v252, s24, 63
	v_writelane_b32 v255, s15, 22
	s_add_u32 s14, s7, s12
	s_addc_u32 s15, s10, 0
	v_writelane_b32 v255, s14, 23
	s_movk_i32 s56, 0x7f
	s_mov_b32 s57, 0xff800000
	v_writelane_b32 v255, s15, 24
	s_add_u32 s14, s8, s12
	s_addc_u32 s15, s9, 0
	s_sub_i32 s11, 0x3d000, s11
	v_writelane_b32 v255, s14, 25
	s_lshl_b32 s11, s11, 1
	s_mov_b32 s65, 0xc2ce8ed0
	v_writelane_b32 v255, s15, 26
	s_add_u32 s14, s7, s11
	s_addc_u32 s15, s10, 0
	s_add_u32 s8, s8, s11
	s_addc_u32 s9, s9, 0
	s_lshl_b32 s5, s5, 8
	s_sub_i32 s4, s4, s5
	s_add_i32 s5, s13, 0xfe00
	s_add_i32 s4, s4, s6
	s_and_b32 s6, s5, 0xffff
	s_mul_i32 s6, s6, 0xaaab
	s_lshr_b32 s7, s6, 21
	s_mul_i32 s7, s7, 48
	s_sub_i32 s5, s5, s7
	v_writelane_b32 v255, s14, 27
	s_and_b32 s7, s5, 0xff
	s_mulk_i32 s7, 0xab
	v_writelane_b32 v255, s15, 28
	v_writelane_b32 v255, s8, 29
	s_bfe_u32 s7, s7, 0x6000a
	s_add_i32 s4, s4, 0x110f00
	v_writelane_b32 v255, s9, 30
	s_mul_i32 s8, s7, 6
	s_sub_i32 s5, s5, s8
	s_and_b32 s5, s5, 0xff
	s_lshl_b32 s7, s7, 12
	s_lshl_b32 s8, s5, 15
	s_add_i32 s7, s7, s8
	v_writelane_b32 v255, s4, 31
	s_bfe_u32 s4, s6, 0x40015
	s_lshl_b32 s6, s7, 7
	s_add_u32 s6, s96, s6
	s_addc_u32 s8, s97, 0
	s_add_u32 s9, s6, 0x5800000
	s_addc_u32 s10, s8, 0
	s_add_u32 s6, s6, 0x7000000
	s_addc_u32 s8, s8, 0
	s_lshl_b32 s11, s4, 7
	s_or_b32 s12, s11, 0x60000
	s_add_u32 s14, s9, s12
	s_addc_u32 s15, s10, 0
	v_writelane_b32 v255, s14, 32
	s_mov_b64 s[44:45], -1
	s_mov_b64 s[86:87], 0x800
	v_writelane_b32 v255, s15, 33
	s_add_u32 s14, s6, s12
	s_addc_u32 s15, s8, 0
	v_writelane_b32 v255, s14, 34
	s_or_b32 s12, s11, 0x40000
	s_mov_b32 s60, 0xbfb8aa3b
	v_writelane_b32 v255, s15, 35
	s_add_u32 s14, s9, s12
	s_addc_u32 s15, s10, 0
	v_writelane_b32 v255, s14, 36
	s_mov_b64 s[88:89], 0x80
	s_mov_b64 s[94:95], 0x100
	v_writelane_b32 v255, s15, 37
	s_add_u32 s14, s6, s12
	s_addc_u32 s15, s8, 0
	v_writelane_b32 v255, s14, 38
	s_or_b32 s12, s11, 0x20000
	s_mov_b32 s62, s67
	v_writelane_b32 v255, s15, 39
	s_add_u32 s14, s9, s12
	s_addc_u32 s15, s10, 0
	v_writelane_b32 v255, s14, 40
	s_nop 1
	v_writelane_b32 v255, s15, 41
	s_add_u32 s14, s6, s12
	s_addc_u32 s15, s8, 0
	v_writelane_b32 v255, s14, 42
	s_nop 1
	v_writelane_b32 v255, s15, 43
	s_add_u32 s14, s9, s11
	s_addc_u32 s15, s10, 0
	v_writelane_b32 v255, s14, 44
	s_add_u32 s10, s6, s11
	s_addc_u32 s11, s8, 0
	v_writelane_b32 v255, s15, 45
	s_lshl_b32 s5, s5, 2
	v_writelane_b32 v255, s10, 46
	s_add_i32 s5, s5, 0
	s_add_i32 s5, s5, 0x21f00
	v_writelane_b32 v255, s11, 47
	v_writelane_b32 v255, s5, 48
	s_ashr_i32 s5, s13, 5
	s_or_b32 s4, s7, s4
	s_sub_i32 s5, 15, s5
	s_lshl_b32 s6, s13, 10
	s_and_b32 s7, s13, 31
	s_and_b32 s6, s6, 0x7000
	s_lshl_b32 s7, s7, 14
	s_or_b32 s14, s4, 0x80000
	s_and_b32 s8, s13, 3
	s_lshl_b32 s16, s5, 8
	s_add_u32 s18, s28, s7
	s_addc_u32 s19, s29, 0
	s_lshl_b32 s7, s5, 2
	v_writelane_b32 v255, s13, 49
	s_or_b32 s20, s7, 3
	s_lshl_b64 s[4:5], s[16:17], 2
	v_writelane_b32 v255, s28, 50
	s_add_u32 s4, s18, s4
	v_writelane_b32 v255, s29, 51
	s_addc_u32 s5, s19, s5
	v_writelane_b32 v255, s4, 52
	s_mov_b32 s15, s67
	s_nop 0
	v_writelane_b32 v255, s5, 53
	s_lshl_b32 s4, s8, 22
	s_lshl_b32 s5, s6, 7
	s_or_b32 s4, s5, s4
	s_add_u32 s4, s96, s4
	s_addc_u32 s5, s97, 0
	s_add_u32 s9, s4, 0x2000000
	s_addc_u32 s10, s5, 0
	s_add_u32 s11, s4, 0x1000000
	s_addc_u32 s12, s5, 0
	s_lshl_b64 s[4:5], s[20:21], 13
	s_add_u32 s22, s11, s4
	s_addc_u32 s23, s12, s5
	v_writelane_b32 v255, s22, 54
	s_add_u32 s4, s9, s4
	s_addc_u32 s5, s10, s5
	v_writelane_b32 v255, s23, 55
	v_writelane_b32 v255, s4, 56
	s_lshl_b32 s66, s20, 6
	s_nop 0
	v_writelane_b32 v255, s5, 57
	s_mov_b32 s4, s20
	v_writelane_b32 v255, s4, 58
	s_nop 1
	v_writelane_b32 v255, s5, 59
	s_lshl_b64 s[4:5], s[66:67], 2
	s_add_u32 s4, s18, s4
	s_addc_u32 s5, s19, s5
; #define LAS __attribute__((address_space(3)))
; #define FOX_ISSUE(i) do { const int j_ = jhi - (i), bf_ = (i) & 3; dma_kv(lds, bf_, Kb + (size_t)j_ * 4096, Vb + (size_t)j_ * 4096, 64, wid, lane); \
;         glds4(cum + j_ * 64 + lane, (unsigned)__builtin_amdgcn_readfirstlane(l0 + L_CK + bf_ * 256)); } while (0)
;     ...
;     bf16x8 qr[4];
;     float fox_cr = 0.f, fox_cv = 0.f, fox_cq = 0.f;
;     auto prologue = [&](int u) {
;         if (!UNIT_ON(u)) return;
;         int lane = tid & 63; asm volatile("" : "+v"(lane));
;         const int r32 = lane & 31, hi = lane >> 5;
;         if (u < AT_NFOX) {
;             const int qb = 15 - (u >> 5), bh = u & 31, b = bh >> 2, h = bh & 3, q0 = qb * 256;
;             const size_t rb = (size_t)b * S;
;             const bf16_t* Kb = proj + ((size_t)(4 + h) * NTOK + rb) * 64;
;             const bf16_t* Vb = proj + ((size_t)(8 + h) * NTOK + rb) * 64;
;             const float* cum = cumall + (size_t)bh * S;
;             const int jhi = 4 * qb + 3;
;             fox_cr = cum[q0]; fox_cv = cum[64 * (lane <= jhi ? lane : jhi) + 63]; fox_cq = cum[q0 + 32 * wid + r32];
;             if (!(dbg & 1)) { FOX_ISSUE(0); FOX_ISSUE(1); FOX_ISSUE(2); }
;             const bf16_t* Q = proj + ((size_t)(0 + h) * NTOK + rb + q0 + 32 * wid + r32) * 64;
; #pragma unroll
;             for (int d0 = 0; d0 < 4; ++d0) qr[d0] = *(const bf16x8*)(Q + d0 * 16 + hi * 8);
; __device__ __forceinline__ void op_mfma(const Args& a, LAS unsigned char* lds, int layer, bf16_t* outp = nullptr) {
;     pg8::DenseOrder So; So.init(a.ws + WS_ACT, a.ws + WS_WOUT + (size_t)layer * D * D * 2, NTOK, D, D, gridDim.x, blockIdx.x, (size_t)256 * 128);
;     bf16_t* xb = (bf16_t*)(a.ws + WS_XB);
;     EpiOut E{layer == 0 ? a.in[I_X] : nullptr, xb, outp ? outp : xb, (const float*)(a.ws + WS_MOD) + (size_t)layer * NB * 6144 + 2048};
;     pg8::gemm_phase<EpiOut, pg8::DenseOrder>(lds, D, So, E, 128u, (size_t)NTOK * 128);
	v_writelane_b32 v255, s4, 60
	s_or_b32 s66, s7, 2
	s_nop 0
	v_writelane_b32 v255, s5, 61
	s_lshl_b64 s[4:5], s[66:67], 13
	s_add_u32 s20, s11, s4
	s_addc_u32 s21, s12, s5
	s_add_u32 s4, s9, s4
	s_addc_u32 s5, s10, s5
	v_writelane_b32 v253, s4, 0
	s_lshl_b32 s66, s66, 6
	v_writelane_b32 v255, s20, 62
	v_writelane_b32 v253, s5, 1
	s_lshl_b64 s[4:5], s[66:67], 2
	s_add_u32 s4, s18, s4
	s_addc_u32 s5, s19, s5
	v_writelane_b32 v253, s4, 2
	s_or_b32 s66, s7, 1
	v_writelane_b32 v255, s21, 63
	v_writelane_b32 v253, s5, 3
	s_lshl_b64 s[4:5], s[66:67], 13
	s_add_u32 s20, s11, s4
	s_addc_u32 s21, s12, s5
	v_writelane_b32 v253, s20, 4
	s_add_u32 s4, s9, s4
	s_addc_u32 s5, s10, s5
	v_writelane_b32 v253, s21, 5
	v_writelane_b32 v253, s4, 6
	s_lshl_b32 s66, s66, 6
	s_mov_b32 s9, s67
	v_writelane_b32 v253, s5, 7
	s_lshl_b64 s[4:5], s[66:67], 2
	s_add_u32 s4, s18, s4
	v_writelane_b32 v253, s18, 8
	s_addc_u32 s5, s19, s5
	s_nop 0
	v_writelane_b32 v253, s19, 9
	v_writelane_b32 v253, s4, 10
	s_nop 1
	v_writelane_b32 v253, s5, 11
	s_lshl_b32 s4, s8, 15
	s_or_b32 s4, s6, s4
	s_mov_b32 s6, s16
	v_writelane_b32 v253, s6, 12
	s_add_i32 s4, s4, s16
	s_mov_b32 s8, s77
	v_writelane_b32 v253, s7, 13
	s_mov_b32 s6, s61
	s_mov_b32 s7, s67
	v_writelane_b32 v253, s4, 14
	s_lshl_b64 s[4:5], s[6:7], 9
	s_lshl_b64 s[70:71], s[8:9], 9
	v_writelane_b32 v253, s4, 15
	s_nop 1
	v_writelane_b32 v253, s5, 16
	s_add_u32 s4, s92, 0x8c00000
	s_addc_u32 s5, s93, 0
	v_writelane_b32 v253, s4, 17
	s_nop 1
	v_writelane_b32 v253, s5, 18
	s_add_u32 s4, s92, 0x1700000
	v_writelane_b32 v253, s4, 19
	s_addc_u32 s4, s93, 0
	v_writelane_b32 v253, s4, 20
	s_add_u32 s4, s92, 0x10000
	v_writelane_b32 v253, s4, 21
	s_addc_u32 s4, s93, 0
	v_writelane_b32 v253, s4, 22
	s_add_u32 s4, s92, 0x300000
	s_addc_u32 s5, s93, 0
	v_writelane_b32 v253, s4, 23
	s_nop 1
	v_writelane_b32 v253, s5, 24
	s_add_u32 s4, s92, 0x500000
	s_addc_u32 s5, s93, 0
	v_writelane_b32 v253, s4, 25
	s_cmpk_lt_i32 s61, 0x100
	s_nop 0
	v_writelane_b32 v253, s5, 26
	s_cselect_b64 s[4:5], -1, 0
	v_writelane_b32 v253, s4, 27
	s_nop 1
	v_writelane_b32 v253, s5, 28
	s_add_u32 s4, s92, 0x14400000
	s_addc_u32 s5, s93, 0
	v_writelane_b32 v253, s4, 29
	s_nop 1
	v_writelane_b32 v253, s5, 30
	s_add_i32 s4, s77, s61
	v_writelane_b32 v253, s4, 31
	s_add_u32 s4, s92, 0x7c00080
	s_addc_u32 s5, s93, 0
	s_add_i32 s2, s3, s2
	s_ashr_i32 s3, s2, 31
	s_lshr_b32 s3, s3, 27
	v_writelane_b32 v253, s4, 32
	s_add_i32 s3, s2, s3
	s_nop 0
	v_writelane_b32 v253, s5, 33
	s_and_b32 s4, s3, 0xffe0
	s_sub_i32 s2, s2, s4
	s_bfe_i32 s4, s2, 0x80000
	s_bfe_u32 s4, s4, 0x3000c
	s_add_i32 s4, s2, s4
	s_and_b32 s5, s4, 0xf8
	s_sub_i32 s2, s2, s5
	s_ashr_i32 s3, s3, 5
	s_bfe_i32 s4, s4, 0x80000
	s_lshl_b32 s3, s3, 3
	s_sext_i32_i16 s4, s4
	s_sext_i32_i8 s2, s2
	s_add_i32 s10, s3, s2
	s_ashr_i32 s2, s4, 3
	v_writelane_b32 v253, s2, 34
	s_lshr_b32 s2, s4, 3
	s_mov_b32 s4, s10
	s_ashr_i32 s11, s10, 31
	v_writelane_b32 v253, s4, 35
	s_nop 1
	v_writelane_b32 v253, s5, 36
	s_lshl_b64 s[4:5], s[10:11], 15
	s_add_u32 s4, s80, s4
	s_addc_u32 s5, s81, s5
	v_writelane_b32 v253, s14, 37
	s_bfe_i64 s[2:3], s[2:3], 0x100000
	s_lshl_b64 s[2:3], s[2:3], 19
	v_writelane_b32 v253, s15, 38
	v_writelane_b32 v253, s2, 39
	s_nop 1
	v_writelane_b32 v253, s3, 40
	s_add_u32 s2, s4, 0x4000
	s_addc_u32 s3, s5, 0
	v_writelane_b32 v253, s2, 41
	s_nop 1
	v_writelane_b32 v253, s3, 42
	s_add_u32 s2, s4, 0x400000
	v_writelane_b32 v253, s4, 43
	s_addc_u32 s3, s5, 0
	s_lshl_b64 s[52:53], s[8:9], 10
	v_writelane_b32 v253, s5, 44
	v_writelane_b32 v253, s2, 45
	s_add_i32 s64, 0, 0x13000
	s_nop 0
	v_writelane_b32 v253, s3, 46
	s_lshl_b32 s2, s61, 7
	v_writelane_b32 v253, s2, 47
	s_lshl_b32 s2, s77, 7
	v_writelane_b32 v253, s2, 48
	s_mul_i32 s2, s77, 0x3000
	v_writelane_b32 v253, s2, 49
	s_add_i32 s2, 0, 0x21c20
	v_writelane_b32 v253, s2, 50
	s_add_i32 s2, 0, 0x21c24
	v_writelane_b32 v253, s2, 51
	s_add_i32 s2, 0, 0x21000
	v_writelane_b32 v253, s2, 52
	s_add_i32 s2, 0, 0x21100
	v_writelane_b32 v253, s2, 53
	s_add_i32 s2, 0, 0x21200
	v_writelane_b32 v253, s2, 54
	s_add_i32 s2, 0, 0x21504
	v_writelane_b32 v253, s2, 55
	s_add_i32 s2, 0, 0x15040
	v_writelane_b32 v253, s2, 56
	s_add_i32 s2, 0, 0x15000
	v_writelane_b32 v253, s2, 57
	s_add_i32 s2, 0, 0x21e80
	v_writelane_b32 v253, s2, 58
	s_add_i32 s2, 0, 0x21e10
	v_writelane_b32 v253, s2, 59
	s_add_i32 s2, 0, 0x21e20
	v_writelane_b32 v253, s2, 60
	s_add_i32 s2, 0, 0x21e30
	v_writelane_b32 v253, s2, 61
	v_writelane_b32 v253, s54, 62
	s_load_dwordx2 s[4:5], s[54:55], 0x0
	s_mov_b32 s3, 0x42b17218
	v_writelane_b32 v253, s55, 63
	s_waitcnt lgkmcnt(0)
	v_writelane_b32 v254, s4, 0
	s_nop 1
	v_writelane_b32 v254, s5, 1
	s_lshl_b64 s[4:5], s[8:9], 13
	v_writelane_b32 v254, s4, 2
	s_nop 1
	v_writelane_b32 v254, s5, 3
	v_writelane_b32 v254, s6, 4
	s_lshl_b64 s[4:5], s[6:7], 12
	s_nop 0
	v_writelane_b32 v254, s7, 5
	v_writelane_b32 v254, s4, 6
	s_nop 1
	v_writelane_b32 v254, s5, 7
	s_lshl_b64 s[4:5], s[8:9], 14
	v_writelane_b32 v254, s4, 8
	s_nop 1
	v_writelane_b32 v254, s5, 9
	v_writelane_b32 v254, s8, 10
	s_lshl_b64 s[4:5], s[8:9], 12
	s_nop 0
	v_writelane_b32 v254, s9, 11
	v_writelane_b32 v254, s4, 12
	s_nop 1
	v_writelane_b32 v254, s5, 13
	v_writelane_b32 v254, s82, 14
	s_nop 1
	v_writelane_b32 v254, s83, 15
	s_branch .LBB0_104

; __device__ __forceinline__ unsigned xb_add(unsigned* p, unsigned v) { return __hip_atomic_fetch_add(p, v, __ATOMIC_RELAXED, __HIP_MEMORY_SCOPE_AGENT); }
; __device__ __forceinline__ void xcd_barrier(const XcdBarrier& b) {
;     asm volatile("s_waitcnt vmcnt(0)" ::: "memory");
;     __syncthreads();
;     if (threadIdx.x == 0) {
;         unsigned* bar = b.bar; unsigned bx = b.x;
;         asm volatile("" : "+s"(bar), "+s"(bx));
;         __builtin_amdgcn_s_waitcnt(0);
;         unsigned nloc = b.st[0], nx = b.st[1];
;         if (nloc == 0u) { xcd_barrier_complete(bar, bx, nloc, nx); b.st[0] = nloc; b.st[1] = nx; }
;         const unsigned old = xb_add(&bar[XB_XSUB(bx)], 1u);
.LBB0_346:
	v_readlane_b32 vcc_lo, v254, 60
	s_nop 1
	s_cmp_eq_u32 vcc_lo, 1
	s_cbranch_scc1 .Ldn_prep_ret
	s_waitcnt vmcnt(0)
	s_waitcnt vmcnt(0)
	s_barrier
	s_mov_b64 s[38:39], exec
	v_readlane_b32 s4, v252, 3
	v_readlane_b32 s5, v252, 4
	s_and_b64 s[4:5], s[38:39], s[4:5]
	s_mov_b64 exec, s[4:5]
	s_cbranch_execz .LBB0_390
	v_readlane_b32 s40, v252, 0
	v_readlane_b32 s4, v253, 50
	v_readlane_b32 s41, v252, 1
	v_readlane_b32 s2, v252, 2
	v_mov_b32_e32 v1, s4
	s_waitcnt vmcnt(0) expcnt(0) lgkmcnt(0)
	ds_read_b32 v4, v1
	v_readlane_b32 s4, v253, 51
	s_waitcnt lgkmcnt(0)
	v_cmp_ne_u32_e32 vcc, 0, v4
	v_mov_b32_e32 v1, s4
	ds_read_b32 v2, v1
	s_cbranch_vccnz .LBB0_361
	v_readlane_b32 s4, v252, 5
	v_readlane_b32 s5, v252, 6
	s_load_dwordx2 s[8:9], s[4:5], 0x4
	s_add_u32 s4, s40, 0x1000
	s_addc_u32 s5, s41, 0
	s_add_u32 s6, s40, 0x1100
	s_addc_u32 s7, s41, 0
	s_waitcnt lgkmcnt(0)
	s_mul_i32 s30, s8, s77
	s_add_u32 s8, s40, 0x1200
	s_mul_i32 s30, s30, s9
	s_addc_u32 s9, s41, 0
	s_add_u32 s10, s40, 0x1300
	s_addc_u32 s11, s41, 0
	s_mov_b32 s31, 1
	s_mov_b64 s[12:13], 0
	s_branch .LBB0_351

; #define LAS __attribute__((address_space(3)))
; __device__ __forceinline__ int opaque_tid() { int t = threadIdx.x; asm volatile("" : "+v"(t)); return t; }
;     const int tid = opaque_tid(), lane = tid & 63, wave = tid >> 6;
;     LAS float* scr = (LAS float*)(lds + 49152) + wave * (64 * 33);
;     const int gw = ((int)blockIdx.x - blk0) * NWAVES + wave, ngw = nblk * NWAVES;
;     constexpr int I_L = 16 * 104 + 16 * 32 + 16 * 16 * 32 + 16 * 8 * 32;
;     if ((int)blockIdx.x < blk0 || (int)blockIdx.x >= blk0 + nblk) return;
;     float tv[32];
;     const int I_E = it_hi < I_L ? it_hi : I_L;
;     int it = it_lo + gw;
;     if (it < I_E) { const PrepItem p = prep_decode(a, l, it);
; #pragma unroll
;         for (int i = 0; i < 32; ++i) tv[i] = __builtin_nontemporal_load(p.src + (size_t)(2 * i + (lane >> 5)) * p.ldw + (lane & 31)); }
; __device__ __forceinline__ void dn_mfma(const Args& a, LAS unsigned char* lds, int layer) {
;     seg_to_lds(a, lds, layer);
;     const LAS int* seg = (const LAS int*)(lds + SEG_OFF);
;     pg8::GroupedOrder So{(const char*)(a.ws + WS_HID), (const char*)(a.ws + WS_WDN + (size_t)layer * NE * 1024 * DFF * 2), seg, 4, (int)gridDim.x, (int)blockIdx.x, (size_t)DFF * 2, (size_t)1024 * DFF * 2, (size_t)256 * DFF * 2};
;     EpiDown E{(bf16_t*)(a.ws + WS_YBUF), (const int*)(a.ws + WS_LIST), (const float*)(a.ws + WS_LISTW), seg, lds};
;     pg8::gemm_phase<EpiDown, pg8::GroupedOrder>(lds, DFF, So, E);
; }
.LBB0_1321:
	v_readlane_b32 vcc_lo, v254, 16
	s_nop 1
	s_cmp_lg_u32 vcc_lo, 0
	s_cbranch_scc1 .Ldn_prep_skip
	v_readlane_b32 s4, v254, 63
	s_nop 1
	s_add_i32 s4, s4, 64
	s_cmpk_eq_u32 s77, 0x100
	s_cselect_b32 s4, s4, 0
	s_sub_i32 s5, s77, s4
	s_cmp_ge_u32 s61, s4
	s_cselect_b64 s[6:7], -1, 0
	s_sub_i32 s8, s61, s4
	s_lshl_b32 s8, s8, 3
	s_addk_i32 s8, 0x2880
	s_lshl_b32 s5, s5, 3
	s_movk_i32 s9, 0x3880
	s_mov_b32 s10, 1
	s_nop 0
	v_writelane_b32 v252, s9, 36
	v_writelane_b32 v252, s5, 37
	v_writelane_b32 v252, s6, 38
	v_writelane_b32 v252, s7, 39
	v_writelane_b32 v252, s8, 40
	v_writelane_b32 v254, s10, 60
	v_mov_b32_e32 v112, v57
	s_mov_b64 s[44:45], -1
	s_branch .LBB0_302
.Ldn_prep_ret:
	s_mov_b32 vcc_lo, 0
	v_mov_b32_e32 v57, v112
	v_writelane_b32 v254, vcc_lo, 60
